# nt hint also on the router phase's residual-row reads and the adaLN weight reads
# speedup vs baseline: 1.0051x; 1.0034x over previous
.LBB0_77:
	v_add_co_u32_e64 v76, s[4:5], s14, v58
	ds_read_b128 v[6:9], v87
	ds_read_b128 v[2:5], v87 offset:16
	v_addc_co_u32_e64 v77, s[4:5], -1, v59, s[4:5]
	v_add_co_u32_e64 v78, s[4:5], s15, v58
	v_add_u32_e32 v85, 0x10000, v87
	s_nop 0
	v_addc_co_u32_e64 v79, s[4:5], -1, v59, s[4:5]
	v_add_co_u32_e64 v80, s[4:5], s16, v58
	global_load_dword v84, v[58:59], off nt
	s_nop 0
	v_addc_co_u32_e64 v81, s[4:5], -1, v59, s[4:5]
	v_add_co_u32_e64 v82, s[4:5], s17, v58
	ds_read_b128 v[14:17], v87 offset:4096
	ds_read_b128 v[10:13], v87 offset:4112
	ds_read_b128 v[90:93], v87 offset:8192
	ds_read_b128 v[46:49], v87 offset:8208
	ds_read_b128 v[22:25], v87 offset:12288
	ds_read_b128 v[18:21], v87 offset:12304
	ds_read_b128 v[94:97], v87 offset:16384
	ds_read_b128 v[98:101], v87 offset:16400
	ds_read_b128 v[30:33], v87 offset:20480
	ds_read_b128 v[26:29], v87 offset:20496
	ds_read_b128 v[102:105], v87 offset:24576
	ds_read_b128 v[106:109], v87 offset:24592
	ds_read_b128 v[38:41], v87 offset:28672
	ds_read_b128 v[34:37], v87 offset:28688
	ds_read_b128 v[110:113], v87 offset:32768
	ds_read_b128 v[114:117], v87 offset:32784
	ds_read_b128 v[118:121], v87 offset:36864
	ds_read_b128 v[42:45], v87 offset:36880
	ds_read_b128 v[122:125], v87 offset:40960
	ds_read_b128 v[126:129], v87 offset:40976
	ds_read_b128 v[130:133], v87 offset:45056
	ds_read_b128 v[134:137], v87 offset:45072
	ds_read_b128 v[138:141], v87 offset:49152
	ds_read_b128 v[142:145], v87 offset:49168
	ds_read_b128 v[146:149], v87 offset:53248
	ds_read_b128 v[150:153], v87 offset:53264
	ds_read_b128 v[154:157], v87 offset:57344
	ds_read_b128 v[158:161], v87 offset:57360
	ds_read_b128 v[162:165], v87 offset:61440
	ds_read_b128 v[166:169], v87 offset:61456
	v_addc_co_u32_e64 v83, s[4:5], -1, v59, s[4:5]
	v_add_co_u32_e64 v170, s[4:5], s12, v58
	global_load_dword v176, v[76:77], off nt
	global_load_dword v178, v[78:79], off nt
	global_load_dword v180, v[80:81], off nt
	global_load_dword v182, v[82:83], off nt
	v_addc_co_u32_e64 v171, s[4:5], 0, v59, s[4:5]
	v_add_co_u32_e64 v172, s[4:5], s18, v58
	ds_read_b128 v[76:79], v85
	s_nop 0
	v_addc_co_u32_e64 v173, s[4:5], 0, v59, s[4:5]
	v_add_co_u32_e64 v174, s[4:5], s19, v58
	v_add_u32_e32 v89, 0x10010, v87
	s_nop 0
	v_addc_co_u32_e64 v175, s[4:5], 0, v59, s[4:5]
	global_load_dword v170, v[170:171], off nt
	s_nop 0
	global_load_dword v172, v[172:173], off nt
	s_nop 0
	global_load_dword v174, v[174:175], off nt
	ds_read_b128 v[80:83], v89
	s_waitcnt lgkmcnt(14)
	v_mov_b32_e32 v185, v14
	v_mov_b32_e32 v14, v7
	v_mov_b32_e32 v7, v16
	v_mov_b32_e32 v16, v9
	v_mov_b32_e32 v9, v22
	v_mov_b32_e32 v22, v91
	v_mov_b32_e32 v91, v24
	v_mov_b32_e32 v24, v93
	v_mov_b32_e32 v93, v30
	v_mov_b32_e32 v30, v95
	v_mov_b32_e32 v95, v32
	v_mov_b32_e32 v32, v97
	v_mov_b32_e32 v97, v38
	v_mov_b32_e32 v38, v103
	v_mov_b32_e32 v103, v40
	v_mov_b32_e32 v40, v105
	v_mov_b32_e32 v105, v118
	v_mov_b32_e32 v118, v111
	v_mov_b32_e32 v111, v120
	v_mov_b32_e32 v120, v113
	s_waitcnt lgkmcnt(11)
	v_mov_b32_e32 v113, v130
	v_mov_b32_e32 v130, v123
	v_mov_b32_e32 v123, v132
	v_mov_b32_e32 v132, v125
	s_waitcnt lgkmcnt(7)
	v_mov_b32_e32 v125, v146
	v_mov_b32_e32 v146, v139
	v_mov_b32_e32 v139, v148
	v_mov_b32_e32 v148, v141
	s_waitcnt lgkmcnt(3)
	v_mov_b32_e32 v141, v162
	v_mov_b32_e32 v162, v155
	v_mov_b32_e32 v184, v6
	v_mov_b32_e32 v6, v8
	v_mov_b32_e32 v8, v90
	v_mov_b32_e32 v90, v92
	v_mov_b32_e32 v92, v94
	v_mov_b32_e32 v94, v96
	v_mov_b32_e32 v96, v102
	v_mov_b32_e32 v102, v104
	v_mov_b32_e32 v104, v110
	v_mov_b32_e32 v110, v112
	v_mov_b32_e32 v112, v122
	v_mov_b32_e32 v122, v124
	v_mov_b32_e32 v124, v138
	v_mov_b32_e32 v138, v140
	v_mov_b32_e32 v140, v154
	v_mov_b32_e32 v154, v156
	v_mov_b32_e32 v155, v164
	v_mov_b32_e32 v164, v157
	v_mov_b32_e32 v156, v2
	v_mov_b32_e32 v157, v10
	v_mov_b32_e32 v10, v3
	v_mov_b32_e32 v2, v4
	v_mov_b32_e32 v3, v12
	v_mov_b32_e32 v12, v5
	v_mov_b32_e32 v4, v46
	v_mov_b32_e32 v5, v18
	v_mov_b32_e32 v18, v47
	v_mov_b32_e32 v46, v48
	v_mov_b32_e32 v47, v20
	v_mov_b32_e32 v20, v49
	v_mov_b32_e32 v48, v98
	v_mov_b32_e32 v49, v26
	v_mov_b32_e32 v26, v99
	v_mov_b32_e32 v98, v100
	v_mov_b32_e32 v99, v28
	v_mov_b32_e32 v28, v101
	v_mov_b32_e32 v100, v106
	v_mov_b32_e32 v101, v34
	v_mov_b32_e32 v34, v107
	v_mov_b32_e32 v106, v108
	v_mov_b32_e32 v107, v36
	v_mov_b32_e32 v36, v109
	v_mov_b32_e32 v108, v114
	v_mov_b32_e32 v109, v42
	v_mov_b32_e32 v42, v115
	v_mov_b32_e32 v114, v116
	v_mov_b32_e32 v115, v44
	v_mov_b32_e32 v44, v117
	v_mov_b32_e32 v116, v126
	v_mov_b32_e32 v117, v134
	v_mov_b32_e32 v134, v127
	v_mov_b32_e32 v126, v128
	v_mov_b32_e32 v127, v136
	v_mov_b32_e32 v136, v129
	v_mov_b32_e32 v128, v142
	v_mov_b32_e32 v129, v150
	v_mov_b32_e32 v150, v143
	v_mov_b32_e32 v142, v144
	v_mov_b32_e32 v143, v152
	v_mov_b32_e32 v152, v145
	v_mov_b32_e32 v144, v158
	s_waitcnt lgkmcnt(2)
	v_mov_b32_e32 v145, v166
	v_mov_b32_e32 v166, v159
	v_mov_b32_e32 v158, v160
	v_mov_b32_e32 v159, v168
	v_mov_b32_e32 v168, v161
	s_waitcnt lgkmcnt(1)
	v_mov_b32_e32 v160, v77
	v_mov_b32_e32 v161, v78
	v_mov_b32_e32 v77, v79
	s_waitcnt lgkmcnt(0)
	v_mov_b32_e32 v78, v81
	v_mov_b32_e32 v79, v82
	v_mov_b32_e32 v81, v83
	s_waitcnt vmcnt(5)
	v_pk_mul_f32 v[14:15], v[178:179], v[14:15] op_sel_hi:[0,1]
	s_waitcnt vmcnt(3)
	v_pk_mul_f32 v[16:17], v[182:183], v[16:17] op_sel_hi:[0,1]
	v_pk_mul_f32 v[22:23], v[178:179], v[22:23] op_sel_hi:[0,1]
	v_pk_mul_f32 v[24:25], v[182:183], v[24:25] op_sel_hi:[0,1]
	v_pk_mul_f32 v[30:31], v[178:179], v[30:31] op_sel_hi:[0,1]
	v_pk_mul_f32 v[32:33], v[182:183], v[32:33] op_sel_hi:[0,1]
	v_pk_mul_f32 v[38:39], v[178:179], v[38:39] op_sel_hi:[0,1]
	v_pk_mul_f32 v[40:41], v[182:183], v[40:41] op_sel_hi:[0,1]
	v_pk_mul_f32 v[82:83], v[178:179], v[118:119] op_sel_hi:[0,1]
	v_pk_mul_f32 v[118:119], v[182:183], v[120:121] op_sel_hi:[0,1]
	v_pk_mul_f32 v[120:121], v[178:179], v[130:131] op_sel_hi:[0,1]
	v_pk_mul_f32 v[130:131], v[182:183], v[132:133] op_sel_hi:[0,1]
	v_pk_mul_f32 v[132:133], v[178:179], v[146:147] op_sel_hi:[0,1]
	v_pk_mul_f32 v[146:147], v[182:183], v[148:149] op_sel_hi:[0,1]
	v_pk_mul_f32 v[148:149], v[178:179], v[162:163] op_sel_hi:[0,1]
	v_pk_mul_f32 v[162:163], v[182:183], v[164:165] op_sel_hi:[0,1]
	s_waitcnt vmcnt(2)
	v_pk_mul_f32 v[10:11], v[170:171], v[10:11] op_sel_hi:[0,1]
	s_waitcnt vmcnt(0)
	v_pk_mul_f32 v[12:13], v[174:175], v[12:13] op_sel_hi:[0,1]
	v_pk_mul_f32 v[18:19], v[170:171], v[18:19] op_sel_hi:[0,1]
	v_pk_mul_f32 v[20:21], v[174:175], v[20:21] op_sel_hi:[0,1]
	v_pk_mul_f32 v[26:27], v[170:171], v[26:27] op_sel_hi:[0,1]
	v_pk_mul_f32 v[28:29], v[174:175], v[28:29] op_sel_hi:[0,1]
	v_pk_mul_f32 v[34:35], v[170:171], v[34:35] op_sel_hi:[0,1]
	v_pk_mul_f32 v[36:37], v[174:175], v[36:37] op_sel_hi:[0,1]
	v_pk_mul_f32 v[42:43], v[170:171], v[42:43] op_sel_hi:[0,1]
	v_pk_mul_f32 v[44:45], v[174:175], v[44:45] op_sel_hi:[0,1]
	v_pk_mul_f32 v[134:135], v[170:171], v[134:135] op_sel_hi:[0,1]
	v_pk_mul_f32 v[150:151], v[170:171], v[150:151] op_sel_hi:[0,1]
	v_pk_mul_f32 v[164:165], v[170:171], v[166:167] op_sel_hi:[0,1]
	v_pk_fma_f32 v[14:15], v[176:177], v[184:185], v[14:15] op_sel_hi:[0,1,1]
	v_pk_fma_f32 v[6:7], v[180:181], v[6:7], v[16:17] op_sel_hi:[0,1,1]
	v_pk_fma_f32 v[8:9], v[176:177], v[8:9], v[22:23] op_sel_hi:[0,1,1]
	v_pk_fma_f32 v[16:17], v[180:181], v[90:91], v[24:25] op_sel_hi:[0,1,1]
	v_pk_fma_f32 v[22:23], v[176:177], v[92:93], v[30:31] op_sel_hi:[0,1,1]
	v_pk_fma_f32 v[24:25], v[180:181], v[94:95], v[32:33] op_sel_hi:[0,1,1]
	v_pk_fma_f32 v[30:31], v[176:177], v[96:97], v[38:39] op_sel_hi:[0,1,1]
	v_pk_fma_f32 v[32:33], v[180:181], v[102:103], v[40:41] op_sel_hi:[0,1,1]
	v_pk_fma_f32 v[38:39], v[176:177], v[104:105], v[82:83] op_sel_hi:[0,1,1]
	v_pk_fma_f32 v[40:41], v[180:181], v[110:111], v[118:119] op_sel_hi:[0,1,1]
	v_pk_fma_f32 v[82:83], v[176:177], v[112:113], v[120:121] op_sel_hi:[0,1,1]
	v_pk_fma_f32 v[92:93], v[176:177], v[124:125], v[132:133] op_sel_hi:[0,1,1]
	v_pk_fma_f32 v[96:97], v[176:177], v[140:141], v[148:149] op_sel_hi:[0,1,1]
	v_mov_b32_e32 v177, v182
	v_mov_b32_e32 v179, v180
	v_pk_fma_f32 v[10:11], v[84:85], v[156:157], v[10:11] op_sel_hi:[0,1,1]
	v_pk_fma_f32 v[2:3], v[172:173], v[2:3], v[12:13] op_sel_hi:[0,1,1]
	v_pk_fma_f32 v[4:5], v[84:85], v[4:5], v[18:19] op_sel_hi:[0,1,1]
	v_pk_fma_f32 v[12:13], v[172:173], v[46:47], v[20:21] op_sel_hi:[0,1,1]
	v_pk_fma_f32 v[18:19], v[84:85], v[48:49], v[26:27] op_sel_hi:[0,1,1]
	v_pk_fma_f32 v[20:21], v[172:173], v[98:99], v[28:29] op_sel_hi:[0,1,1]
	v_pk_fma_f32 v[26:27], v[84:85], v[100:101], v[34:35] op_sel_hi:[0,1,1]
	v_pk_fma_f32 v[28:29], v[172:173], v[106:107], v[36:37] op_sel_hi:[0,1,1]
	v_pk_fma_f32 v[34:35], v[84:85], v[108:109], v[42:43] op_sel_hi:[0,1,1]
	v_pk_fma_f32 v[36:37], v[172:173], v[114:115], v[44:45] op_sel_hi:[0,1,1]
	v_pk_fma_f32 v[42:43], v[84:85], v[116:117], v[134:135] op_sel_hi:[0,1,1]
	v_pk_fma_f32 v[46:47], v[84:85], v[128:129], v[150:151] op_sel_hi:[0,1,1]
	v_pk_fma_f32 v[98:99], v[84:85], v[144:145], v[164:165] op_sel_hi:[0,1,1]
	v_mov_b32_e32 v85, v174
	v_pk_add_f32 v[6:7], v[14:15], v[6:7]
	v_pk_add_f32 v[14:15], v[22:23], v[24:25]
	v_pk_add_f32 v[22:23], v[38:39], v[40:41]
	v_pk_mul_f32 v[38:39], v[176:177], v[76:77]
	v_pk_mul_f32 v[136:137], v[174:175], v[136:137] op_sel_hi:[0,1]
	v_pk_mul_f32 v[152:153], v[174:175], v[152:153] op_sel_hi:[0,1]
	v_pk_mul_f32 v[166:167], v[174:175], v[168:169] op_sel_hi:[0,1]
	v_mov_b32_e32 v171, v172
	v_pk_fma_f32 v[90:91], v[180:181], v[122:123], v[130:131] op_sel_hi:[0,1,1]
	v_pk_fma_f32 v[94:95], v[180:181], v[138:139], v[146:147] op_sel_hi:[0,1,1]
	v_pk_fma_f32 v[102:103], v[180:181], v[154:155], v[162:163] op_sel_hi:[0,1,1]
	v_pk_add_f32 v[2:3], v[10:11], v[2:3]
	v_pk_add_f32 v[10:11], v[18:19], v[20:21]
	v_pk_add_f32 v[18:19], v[34:35], v[36:37]
	v_pk_mul_f32 v[34:35], v[84:85], v[80:81]
	v_pk_fma_f32 v[36:37], v[178:179], v[160:161], v[38:39]
	v_pk_fma_f32 v[44:45], v[172:173], v[126:127], v[136:137] op_sel_hi:[0,1,1]
	v_pk_fma_f32 v[48:49], v[172:173], v[142:143], v[152:153] op_sel_hi:[0,1,1]
	v_pk_fma_f32 v[100:101], v[172:173], v[158:159], v[166:167] op_sel_hi:[0,1,1]
	v_pk_add_f32 v[8:9], v[8:9], v[16:17]
	v_pk_add_f32 v[16:17], v[30:31], v[32:33]
	v_pk_add_f32 v[24:25], v[82:83], v[90:91]
	v_pk_add_f32 v[30:31], v[92:93], v[94:95]
	v_pk_add_f32 v[32:33], v[96:97], v[102:103]
	v_pk_add_f32 v[6:7], v[60:61], v[6:7]
	v_pk_fma_f32 v[34:35], v[170:171], v[78:79], v[34:35]
	v_add_f32_e32 v36, v36, v37
	s_add_i32 s8, s8, 8
	v_pk_add_f32 v[4:5], v[4:5], v[12:13]
	v_pk_add_f32 v[12:13], v[26:27], v[28:29]
	v_pk_add_f32 v[20:21], v[42:43], v[44:45]
	v_pk_add_f32 v[26:27], v[46:47], v[48:49]
	v_pk_add_f32 v[28:29], v[98:99], v[100:101]
	v_pk_add_f32 v[8:9], v[62:63], v[8:9]
	v_pk_add_f32 v[14:15], v[64:65], v[14:15]
	v_pk_add_f32 v[16:17], v[66:67], v[16:17]
	v_pk_add_f32 v[22:23], v[68:69], v[22:23]
	v_pk_add_f32 v[24:25], v[70:71], v[24:25]
	v_pk_add_f32 v[30:31], v[72:73], v[30:31]
	v_pk_add_f32 v[32:33], v[74:75], v[32:33]
	v_pk_add_f32 v[60:61], v[6:7], v[2:3]
	v_add_f32_e32 v2, v34, v35
	v_add_f32_e32 v3, v88, v36
	v_add_u32_e32 v87, 32, v87
	v_lshl_add_u64 v[58:59], v[58:59], 0, s[2:3]
	s_cmpk_gt_u32 s8, 0x7b
	v_pk_add_f32 v[62:63], v[8:9], v[4:5]
	v_pk_add_f32 v[64:65], v[14:15], v[10:11]
	v_pk_add_f32 v[66:67], v[16:17], v[12:13]
	v_pk_add_f32 v[68:69], v[22:23], v[18:19]
	v_pk_add_f32 v[70:71], v[24:25], v[20:21]
	v_pk_add_f32 v[72:73], v[30:31], v[26:27]
	v_pk_add_f32 v[74:75], v[32:33], v[28:29]
	v_add_f32_e32 v88, v3, v2
	s_cbranch_scc0 .LBB0_77
	ds_write2st64_b32 v52, v60, v61 offset1:1
	ds_write2st64_b32 v52, v62, v63 offset0:2 offset1:3
	ds_write2st64_b32 v52, v64, v65 offset0:4 offset1:5
	ds_write2st64_b32 v52, v66, v67 offset0:6 offset1:7
	ds_write2st64_b32 v52, v68, v69 offset0:8 offset1:9
	ds_write2st64_b32 v52, v70, v71 offset0:10 offset1:11
	ds_write2st64_b32 v52, v72, v73 offset0:12 offset1:13
	ds_write2st64_b32 v52, v74, v75 offset0:14 offset1:15
	ds_write_b32 v52, v88 offset:4096
	s_waitcnt lgkmcnt(0)
	s_barrier
	s_and_saveexec_b64 s[8:9], vcc
	s_cbranch_execz .LBB0_75
	s_mul_i32 s4, s10, 0xffffffa0
	s_add_i32 s4, s4, s27
	s_lshl_b32 s4, s4, 6
	s_add_i32 s11, s4, s11
	v_or_b32_e32 v2, s11, v1
	s_ashr_i32 s5, s4, 31
	v_ashrrev_i32_e32 v3, 31, v2
	s_mul_i32 s21, s10, 17
	v_lshl_add_u64 v[2:3], v[2:3], 2, s[6:7]
	v_lshl_add_u64 v[4:5], s[4:5], 2, v[54:55]
	s_mov_b64 s[10:11], 0
	v_mov_b32_e32 v6, v50

.LBB0_922:
	s_add_i32 s26, s4, s2
	s_ashr_i32 s6, s26, 12
	s_mulk_i32 s6, 0x1100
	s_add_i32 s27, s6, 0x100
	s_and_b32 s6, s26, 0xffc
	v_readlane_b32 vcc_lo, v252, 6
	s_add_i32 s28, s27, s6
	v_readlane_b32 vcc_hi, v252, 7
	s_and_b64 s[6:7], vcc, exec
	s_cselect_b32 s70, s26, s28
	s_mul_hi_i32 s6, s70, 0x78787879
	s_lshr_b32 s7, s6, 31
	s_ashr_i32 s6, s6, 11
	s_add_i32 s6, s6, s7
	s_mul_i32 s7, s6, 0xffffef00
	s_add_i32 s7, s7, s70
	s_cmpk_gt_i32 s7, 0xff
	s_cselect_b32 s33, s6, 16
	s_ashr_i32 s71, s70, 31
	s_lshl_b64 s[64:65], s[70:71], 11
	v_lshl_add_u64 v[32:33], v[58:59], 0, s[64:65]
	global_load_dwordx4 v[70:73], v[32:33], off nt
	global_load_dwordx4 v[74:77], v[32:33], off offset:1024 nt
	s_add_i32 s28, s26, 1
	s_and_b32 s6, s28, 0xffd
	s_add_i32 s29, s27, s6
	s_and_b64 s[6:7], vcc, exec
	s_cselect_b32 s48, s28, s29
	s_add_i32 s28, s26, 2
	s_ashr_i32 s49, s48, 31
	s_and_b32 s6, s28, 0xffe
	s_lshl_b64 s[46:47], s[48:49], 11
	s_add_i32 s29, s27, s6
	s_and_b64 s[6:7], vcc, exec
	s_cselect_b32 s42, s28, s29
	s_add_i32 s26, s26, 3
	s_ashr_i32 s43, s42, 31
	s_and_b32 s6, s26, 0xfff
	s_lshl_b64 s[40:41], s[42:43], 11
	s_add_i32 s27, s27, s6
	s_and_b64 s[6:7], vcc, exec
	s_cselect_b32 s26, s26, s27
	v_lshl_add_u64 v[32:33], v[58:59], 0, s[46:47]
	s_ashr_i32 s27, s26, 31
	global_load_dwordx4 v[52:55], v[32:33], off nt
	global_load_dwordx4 v[48:51], v[32:33], off offset:1024 nt
	v_lshl_add_u64 v[32:33], v[58:59], 0, s[40:41]
	s_lshl_b64 s[6:7], s[26:27], 11
	global_load_dwordx4 v[44:47], v[32:33], off nt
	global_load_dwordx4 v[40:43], v[32:33], off offset:1024 nt
	v_lshl_add_u64 v[32:33], v[58:59], 0, s[6:7]
	global_load_dwordx4 v[36:39], v[32:33], off nt
	s_nop 0
	global_load_dwordx4 v[32:35], v[32:33], off offset:1024 nt
	s_cmp_eq_u32 s33, s14
	s_waitcnt vmcnt(7)
	v_and_b32_e32 v97, 0xffff0000, v70
	v_and_b32_e32 v93, 0xffff0000, v71
	v_lshlrev_b32_e32 v96, 16, v70
	v_lshlrev_b32_e32 v92, 16, v71
	v_mul_f32_e32 v70, v97, v97
	v_mul_f32_e32 v71, v93, v93
	v_and_b32_e32 v89, 0xffff0000, v72
	v_and_b32_e32 v87, 0xffff0000, v73
	v_fmac_f32_e32 v70, v96, v96
	v_fmac_f32_e32 v71, v92, v92
	v_lshlrev_b32_e32 v88, 16, v72
	v_lshlrev_b32_e32 v86, 16, v73
	v_add_f32_e32 v70, v70, v71
	v_mul_f32_e32 v71, v89, v89
	v_mul_f32_e32 v72, v87, v87
	v_fmac_f32_e32 v71, v88, v88
	v_fmac_f32_e32 v72, v86, v86
	v_add_f32_e32 v71, v71, v72
	s_waitcnt vmcnt(6)
	v_and_b32_e32 v83, 0xffff0000, v74
	v_and_b32_e32 v85, 0xffff0000, v75
	v_add_f32_e32 v70, v70, v71
	v_lshlrev_b32_e32 v82, 16, v74
	v_lshlrev_b32_e32 v84, 16, v75
	v_mul_f32_e32 v71, v83, v83
	v_mul_f32_e32 v72, v85, v85
	v_and_b32_e32 v79, 0xffff0000, v76
	v_and_b32_e32 v81, 0xffff0000, v77
	v_fmac_f32_e32 v71, v82, v82
	v_fmac_f32_e32 v72, v84, v84
	v_lshlrev_b32_e32 v78, 16, v76
	v_lshlrev_b32_e32 v80, 16, v77
	v_add_f32_e32 v71, v71, v72
	v_mul_f32_e32 v72, v79, v79
	v_mul_f32_e32 v73, v81, v81
	v_fmac_f32_e32 v72, v78, v78
	v_fmac_f32_e32 v73, v80, v80
	v_add_f32_e32 v72, v72, v73
	v_add_f32_e32 v71, v71, v72
	v_add_f32_e32 v70, v70, v71
	s_nop 1
	v_mov_b32_dpp v71, v70 quad_perm:[1,0,3,2] row_mask:0xf bank_mask:0xf
	s_waitcnt lgkmcnt(0)
	v_add_f32_e32 v70, v70, v71
	s_nop 1
	v_mov_b32_dpp v71, v70 quad_perm:[2,3,0,1] row_mask:0xf bank_mask:0xf
	s_waitcnt lgkmcnt(0)
	v_add_f32_e32 v70, v70, v71
	s_nop 1
	v_mov_b32_dpp v71, v70 row_half_mirror row_mask:0xf bank_mask:0xf
	s_waitcnt lgkmcnt(0)
	v_add_f32_e32 v70, v70, v71
	s_nop 1
	v_mov_b32_dpp v71, v70 row_mirror row_mask:0xf bank_mask:0xf
	s_waitcnt lgkmcnt(0)
	v_add_f32_e32 v70, v70, v71
	ds_swizzle_b32 v71, v70 offset:swizzle(SWAP,16)
	s_waitcnt lgkmcnt(0)
	v_add_f32_e32 v104, v70, v71
	v_mov_b32_e32 v105, v104
	s_nop 1
	v_permlane32_swap_b32_e32 v104, v105
	s_cbranch_scc1 .LBB0_924
	s_add_i32 s14, s33, s13
	s_mul_hi_i32 s29, s14, 0x6000
	s_mulk_i32 s14, 0x6000
	s_add_u32 s28, s60, s14
	s_addc_u32 s29, s63, s29
	v_lshl_add_u64 v[16:17], v[56:57], 2, s[28:29]
	v_add_co_u32_e32 v8, vcc, 0x4000, v16
	s_mov_b64 s[28:29], 0x4000
	s_nop 0
	v_addc_co_u32_e32 v9, vcc, 0, v17, vcc
	global_load_dwordx4 v[4:7], v[60:61], off offset:16
	global_load_dwordx4 v[0:3], v[60:61], off
	v_lshl_add_u64 v[28:29], v[16:17], 0, s[28:29]
	global_load_dwordx4 v[8:11], v[8:9], off
	s_nop 0
	global_load_dwordx4 v[12:15], v[28:29], off offset:16
	s_movk_i32 s14, 0x3000
	s_mov_b64 s[28:29], 0x3000
	v_lshl_add_u64 v[70:71], v[16:17], 0, s[28:29]
	s_waitcnt vmcnt(1)
	v_pk_add_f32 v[8:9], v[8:9], 1.0 op_sel_hi:[1,0]
	s_nop 0
	v_pk_mul_f32 v[0:1], v[0:1], v[8:9]
	s_waitcnt vmcnt(0)
	v_pk_add_f32 v[8:9], v[14:15], 1.0 op_sel_hi:[1,0]
	v_pk_add_f32 v[10:11], v[10:11], 1.0 op_sel_hi:[1,0]
	v_pk_mul_f32 v[6:7], v[6:7], v[8:9]
	v_add_co_u32_e32 v8, vcc, s14, v16
	v_pk_mul_f32 v[2:3], v[2:3], v[10:11]
	v_pk_add_f32 v[10:11], v[12:13], 1.0 op_sel_hi:[1,0]
	v_addc_co_u32_e32 v9, vcc, 0, v17, vcc
	v_pk_mul_f32 v[4:5], v[4:5], v[10:11]
	global_load_dwordx4 v[8:11], v[8:9], off
	s_nop 0
	global_load_dwordx4 v[12:15], v[70:71], off offset:16
	global_load_dwordx4 v[20:23], v[60:61], off offset:2064
	global_load_dwordx4 v[16:19], v[60:61], off offset:2048
	global_load_dwordx4 v[24:27], v[28:29], off offset:2064
	s_nop 0
	global_load_dwordx4 v[28:31], v[28:29], off offset:2048
	s_mov_b32 s14, s33
	s_waitcnt vmcnt(1)
	v_pk_add_f32 v[26:27], v[26:27], 1.0 op_sel_hi:[1,0]
	s_waitcnt vmcnt(0)
	v_pk_add_f32 v[30:31], v[30:31], 1.0 op_sel_hi:[1,0]
	v_pk_add_f32 v[28:29], v[28:29], 1.0 op_sel_hi:[1,0]
	v_pk_add_f32 v[24:25], v[24:25], 1.0 op_sel_hi:[1,0]
	v_pk_mul_f32 v[18:19], v[18:19], v[30:31]
	v_pk_mul_f32 v[16:17], v[16:17], v[28:29]
	v_pk_mul_f32 v[22:23], v[22:23], v[26:27]
	v_pk_mul_f32 v[20:21], v[20:21], v[24:25]
	global_load_dwordx4 v[24:27], v[70:71], off offset:2064
	global_load_dwordx4 v[28:31], v[70:71], off offset:2048
